# speedup vs baseline: 1.0199x; 1.0199x over previous
_Z6k_gemmPKfS0_PK15HIP_vector_typeIjLj4EEPDF16_PKh:
	s_load_dwordx2 s[38:39], s[0:1], 0x10
	s_load_dwordx4 s[20:23], s[0:1], 0x0
	s_load_dwordx2 s[40:41], s[0:1], 0x20
	v_readfirstlane_b32 s29, v0
	v_and_b32_e32 v196, 63, v0
	s_lshr_b32 s28, s29, 6
	v_mov_b32_e32 v195, 0
	s_waitcnt lgkmcnt(0)
	s_mov_b64 s[24:25], s[22:23]
	v_cmp_gt_u32_e32 vcc, 32, v0
	v_lshrrev_b32_e32 v198, 4, v0
	v_and_b32_e32 v1, 15, v0
	s_and_saveexec_b64 s[4:5], vcc
	s_cbranch_execz .LBB1_2
	v_mul_u32_u24_e32 v154, 0x4e00, v198
	v_mul_u32_u24_e32 v155, 0x4e0, v1
	v_add3_u32 v158, 0, v154, v155
	v_mov_b32_e32 v154, 0
	v_mov_b32_e32 v155, v154
	v_mov_b32_e32 v156, v154
	v_mov_b32_e32 v157, v154
	ds_write_b128 v158, v[154:157] offset:1200
.LBB1_2:
	s_or_b64 exec, exec, s[4:5]
	s_and_b32 s31, s2, 7
	s_lshr_b32 s33, s2, 3
	s_mul_i32 s2, s31, 0x187
	s_min_u32 s3, s2, 0xaae
	s_add_i32 s2, s2, s33
	s_sub_i32 s35, s3, s2
	s_addk_i32 s35, 0x1c6
	s_ashr_i32 s3, s35, 31
	s_lshr_b32 s3, s3, 26
	s_lshl_b32 s2, s2, 4
	s_lshl_b32 s16, s28, 2
	s_add_i32 s3, s35, s3
	s_add_i32 s34, s16, s2
	s_ashr_i32 s30, s3, 6
	v_lshl_add_u32 v154, v196, 10, s34
	s_mov_b32 s2, 0xc350
	v_cmp_gt_i32_e32 vcc, s30, v196
	v_cmp_gt_i32_e64 s[2:3], s2, v154
	s_and_b64 s[4:5], vcc, s[2:3]
	s_waitcnt lgkmcnt(0)
	s_barrier
	s_and_saveexec_b64 s[2:3], s[4:5]
	s_cbranch_execz .LBB1_4
	v_ashrrev_i32_e32 v155, 31, v154
	v_lshl_add_u64 v[154:155], s[40:41], 0, v[154:155]
	global_load_dword v195, v[154:155], off
.LBB1_4:
	s_or_b64 exec, exec, s[2:3]
	v_mul_lo_u16_e32 v154, 0x75, v196
	v_sub_u16_sdwa v155, v196, v154 dst_sel:DWORD dst_unused:UNUSED_PAD src0_sel:DWORD src1_sel:BYTE_1
	v_lshrrev_b16_e32 v155, 1, v155
	v_and_b32_e32 v155, 0x7f, v155
	s_mul_i32 s2, s28, 0x1380
	s_waitcnt vmcnt(0)
	v_readlane_b32 s14, v195, 0
	s_and_b32 s21, s21, 0xffff
	v_add_u16_sdwa v154, v155, v154 dst_sel:DWORD dst_unused:UNUSED_PAD src0_sel:DWORD src1_sel:BYTE_1
	s_and_b32 s25, s25, 0xffff
	s_add_i32 s17, s2, 0
	s_and_b32 s8, s14, 0xff
	v_lshrrev_b16_e32 v154, 3, v154
	s_cmp_eq_u32 s8, 1
	v_and_b32_e32 v154, 31, v154
	s_cselect_b64 vcc, -1, 0
	s_and_b32 s8, s14, 0xff00
	v_min_u16_e32 v202, 3, v154
	s_cmpk_eq_i32 s8, 0x100
	v_mad_i32_i24 v154, v202, -11, v196
	s_cselect_b64 s[8:9], -1, 0
	s_and_b32 s12, s14, 0xff0000
	v_min_i32_e32 v199, 10, v154
	v_subrev_co_u32_e64 v154, s[10:11], 11, v196
	s_cmp_eq_u32 s12, 0x10000
	v_cmp_gt_u32_e64 s[2:3], 11, v154
	v_subrev_u32_e32 v154, 22, v196
	s_cselect_b64 s[12:13], -1, 0
	s_and_b32 s14, s14, 0xff000000
	v_add_u32_e32 v203, 64, v199
	v_lshlrev_b32_e32 v194, 4, v196
	v_cmp_gt_u32_e64 s[4:5], 11, v154
	v_subrev_u32_e32 v154, 33, v196
	s_mulk_i32 s34, 0x4b0
	s_cmp_eq_u32 s14, 0x1000000
	v_lshlrev_b32_e32 v197, 4, v203
	v_cmp_gt_u32_e64 s[6:7], 11, v154
	v_add_u32_e32 v154, s34, v194
	v_mov_b32_e32 v200, 0xffffff00
	s_cselect_b64 s[14:15], -1, 0
	s_add_i32 s18, s34, 0x4b0
	s_mov_b32 s23, 0x20000
	s_mov_b32 s22, 0x3938700
	v_cndmask_b32_e32 v154, v200, v154, vcc
	v_add_u32_e32 v155, s34, v197
	s_and_b64 vcc, vcc, s[10:11]
	v_add_u32_e32 v156, s18, v194
	s_mov_b32 s26, s22
	s_mov_b32 s27, s23
	s_barrier
	v_cndmask_b32_e32 v155, v200, v155, vcc
	v_cndmask_b32_e64 v156, v200, v156, s[8:9]
	buffer_load_dwordx4 v[186:189], v154, s[20:23], 0 offen nt
	buffer_load_dwordx4 v[174:177], v156, s[20:23], 0 offen nt
	buffer_load_dwordx4 v[178:181], v154, s[24:27], 0 offen nt
	buffer_load_dwordx4 v[166:169], v156, s[24:27], 0 offen nt
	v_add_u32_e32 v154, s18, v197
	s_and_b64 vcc, s[8:9], s[2:3]
	s_add_i32 s8, s34, 0x960
	v_cndmask_b32_e32 v154, v155, v154, vcc
	v_add_u32_e32 v155, s8, v194
	v_add_u32_e32 v156, s8, v197
	s_and_b64 vcc, s[12:13], s[4:5]
	s_add_i32 s8, s34, 0xe10
	v_cndmask_b32_e64 v155, v200, v155, s[12:13]
	v_cndmask_b32_e32 v154, v154, v156, vcc
	v_add_u32_e32 v156, s8, v194
	v_cndmask_b32_e64 v156, v200, v156, s[14:15]
	buffer_load_dwordx4 v[190:193], v155, s[20:23], 0 offen nt
	buffer_load_dwordx4 v[170:173], v156, s[20:23], 0 offen nt
	buffer_load_dwordx4 v[182:185], v155, s[24:27], 0 offen nt
	buffer_load_dwordx4 v[162:165], v156, s[24:27], 0 offen nt
	v_add_u32_e32 v155, s8, v197
	s_and_b64 vcc, s[14:15], s[6:7]
	v_cndmask_b32_e32 v154, v154, v155, vcc
	buffer_load_dwordx4 v[158:161], v154, s[20:23], 0 offen nt
	s_nop 0
	buffer_load_dwordx4 v[154:157], v154, s[24:27], 0 offen nt
	v_mov_b32_e32 v209, 0
	v_lshl_or_b32 v208, s28, 7, v196
	v_ashrrev_i32_e32 v3, 31, v208
	v_mov_b32_e32 v2, v208
	v_lshl_add_u64 v[50:51], v[2:3], 4, s[38:39]
	v_add_u32_e32 v2, 0x200, v208
	v_mov_b32_e32 v3, v209
	v_lshl_add_u64 v[52:53], v[2:3], 4, s[38:39]
	v_ashrrev_i32_e32 v3, 31, v2
	v_lshl_add_u64 v[54:55], v[2:3], 4, s[38:39]
	v_add_u32_e32 v2, 0x400, v208
	v_mov_b32_e32 v3, v209
	v_lshl_add_u64 v[56:57], v[2:3], 4, s[38:39]
	v_ashrrev_i32_e32 v3, 31, v2
	v_lshl_add_u64 v[58:59], v[2:3], 4, s[38:39]
	v_add_u32_e32 v2, 0x600, v208
	v_mov_b32_e32 v3, v209
	v_lshl_add_u64 v[60:61], v[2:3], 4, s[38:39]
	v_ashrrev_i32_e32 v3, 31, v2
	v_lshl_add_u64 v[62:63], v[2:3], 4, s[38:39]
	v_add_u32_e32 v2, 0x800, v208
	v_mov_b32_e32 v3, v209
	v_lshl_add_u64 v[64:65], v[2:3], 4, s[38:39]
	v_ashrrev_i32_e32 v3, 31, v2
	v_lshl_add_u64 v[66:67], v[2:3], 4, s[38:39]
	v_add_u32_e32 v2, 0xa00, v208
	v_mov_b32_e32 v3, v209
	v_lshl_add_u64 v[68:69], v[2:3], 4, s[38:39]
	v_ashrrev_i32_e32 v3, 31, v2
	v_lshl_add_u64 v[70:71], v[2:3], 4, s[38:39]
	v_add_u32_e32 v2, 0xc00, v208
	v_mov_b32_e32 v3, v209
	v_lshl_add_u64 v[74:75], v[2:3], 4, s[38:39]
	v_ashrrev_i32_e32 v3, 31, v2
	v_lshl_add_u64 v[76:77], v[2:3], 4, s[38:39]
	v_add_u32_e32 v2, 0xe00, v208
	v_mov_b32_e32 v3, v209
	v_lshl_add_u64 v[78:79], v[2:3], 4, s[38:39]
	v_ashrrev_i32_e32 v3, 31, v2
	v_lshl_add_u64 v[80:81], v[2:3], 4, s[38:39]
	v_add_u32_e32 v2, 0x1000, v208
	v_mov_b32_e32 v3, v209
	v_lshl_add_u64 v[82:83], v[2:3], 4, s[38:39]
	v_ashrrev_i32_e32 v3, 31, v2
	v_lshl_add_u64 v[84:85], v[2:3], 4, s[38:39]
	v_add_u32_e32 v2, 0x1200, v208
	v_mov_b32_e32 v3, v209
	v_lshl_add_u64 v[86:87], v[2:3], 4, s[38:39]
	v_ashrrev_i32_e32 v3, 31, v2
	v_lshl_add_u64 v[88:89], v[2:3], 4, s[38:39]
	v_add_u32_e32 v2, 0x1400, v208
	v_mov_b32_e32 v3, v209
	v_lshl_add_u64 v[90:91], v[2:3], 4, s[38:39]
	v_ashrrev_i32_e32 v3, 31, v2
	v_lshl_add_u64 v[94:95], v[2:3], 4, s[38:39]
	v_add_u32_e32 v2, 0x1600, v208
	v_mov_b32_e32 v3, v209
	v_lshl_add_u64 v[96:97], v[2:3], 4, s[38:39]
	v_ashrrev_i32_e32 v3, 31, v2
	v_lshl_add_u64 v[98:99], v[2:3], 4, s[38:39]
	v_add_u32_e32 v2, 0x1800, v208
	v_mov_b32_e32 v3, v209
	v_lshl_add_u64 v[100:101], v[2:3], 4, s[38:39]
	v_ashrrev_i32_e32 v3, 31, v2
	v_lshl_add_u64 v[102:103], v[2:3], 4, s[38:39]
	v_add_u32_e32 v2, 0x1a00, v208
	v_mov_b32_e32 v3, v209
	v_lshl_add_u64 v[106:107], v[2:3], 4, s[38:39]
	v_ashrrev_i32_e32 v3, 31, v2
	v_lshl_add_u64 v[110:111], v[2:3], 4, s[38:39]
	v_add_u32_e32 v2, 0x1c00, v208
	v_mov_b32_e32 v3, v209
	v_lshl_add_u64 v[114:115], v[2:3], 4, s[38:39]
	v_ashrrev_i32_e32 v3, 31, v2
	v_lshl_add_u64 v[118:119], v[2:3], 4, s[38:39]
	v_add_u32_e32 v2, 0x1e00, v208
	v_mov_b32_e32 v3, v209
	v_lshl_add_u64 v[122:123], v[2:3], 4, s[38:39]
	v_ashrrev_i32_e32 v3, 31, v2
	v_lshl_add_u64 v[126:127], v[2:3], 4, s[38:39]
	v_add_u32_e32 v2, 0x2000, v208
	v_mov_b32_e32 v3, v209
	v_lshl_add_u64 v[130:131], v[2:3], 4, s[38:39]
	v_ashrrev_i32_e32 v3, 31, v2
	v_lshl_add_u64 v[134:135], v[2:3], 4, s[38:39]
	v_add_u32_e32 v2, 0x2200, v208
	v_mov_b32_e32 v3, v209
	v_lshl_add_u64 v[138:139], v[2:3], 4, s[38:39]
	v_ashrrev_i32_e32 v3, 31, v2
	v_lshl_add_u64 v[72:73], v[208:209], 4, s[38:39]
	v_add_u32_e32 v208, 0x2400, v208
	v_lshl_add_u64 v[142:143], v[2:3], 4, s[38:39]
	v_ashrrev_i32_e32 v3, 31, v208
	v_mov_b32_e32 v2, v208
	v_lshl_add_u64 v[150:151], v[2:3], 4, s[38:39]
	global_load_dwordx4 v[2:5], v[72:73], off
	global_load_dwordx4 v[6:9], v[50:51], off offset:1024
	global_load_dwordx4 v[10:13], v[52:53], off
	global_load_dwordx4 v[14:17], v[54:55], off offset:1024
	global_load_dwordx4 v[18:21], v[56:57], off
	global_load_dwordx4 v[22:25], v[58:59], off offset:1024
	global_load_dwordx4 v[26:29], v[60:61], off
	global_load_dwordx4 v[30:33], v[62:63], off offset:1024
	global_load_dwordx4 v[34:37], v[64:65], off
	global_load_dwordx4 v[38:41], v[66:67], off offset:1024
	global_load_dwordx4 v[42:45], v[68:69], off
	global_load_dwordx4 v[46:49], v[70:71], off offset:1024
	global_load_dwordx4 v[50:53], v[74:75], off
	global_load_dwordx4 v[54:57], v[76:77], off offset:1024
	global_load_dwordx4 v[58:61], v[78:79], off
	global_load_dwordx4 v[62:65], v[80:81], off offset:1024
	global_load_dwordx4 v[66:69], v[82:83], off
	global_load_dwordx4 v[70:73], v[84:85], off offset:1024
	s_nop 0
	global_load_dwordx4 v[74:77], v[86:87], off
	global_load_dwordx4 v[78:81], v[88:89], off offset:1024
	global_load_dwordx4 v[82:85], v[90:91], off
	s_nop 0
	global_load_dwordx4 v[86:89], v[94:95], off offset:1024
	global_load_dwordx4 v[90:93], v[96:97], off
	s_nop 0
	global_load_dwordx4 v[94:97], v[98:99], off offset:1024
	s_nop 0
	global_load_dwordx4 v[98:101], v[100:101], off
	s_nop 0
	global_load_dwordx4 v[102:105], v[102:103], off offset:1024
	s_nop 0
	global_load_dwordx4 v[106:109], v[106:107], off
	s_nop 0
	global_load_dwordx4 v[110:113], v[110:111], off offset:1024
	s_nop 0
	global_load_dwordx4 v[114:117], v[114:115], off
	s_nop 0
	global_load_dwordx4 v[118:121], v[118:119], off offset:1024
	s_nop 0
	global_load_dwordx4 v[122:125], v[122:123], off
	s_nop 0
	global_load_dwordx4 v[126:129], v[126:127], off offset:1024
	s_nop 0
	global_load_dwordx4 v[130:133], v[130:131], off
	s_nop 0
	global_load_dwordx4 v[134:137], v[134:135], off offset:1024
	s_nop 0
	global_load_dwordx4 v[138:141], v[138:139], off
	s_nop 0
	global_load_dwordx4 v[142:145], v[142:143], off offset:1024
	v_lshl_add_u64 v[146:147], v[208:209], 4, s[38:39]
	global_load_dwordx4 v[146:149], v[146:147], off
	s_nop 0
	global_load_dwordx4 v[150:153], v[150:151], off offset:1024
	v_or_b32_e32 v202, s16, v202
	s_movk_i32 s12, 0x4e0
	v_lshrrev_b32_e32 v201, 4, v196
	v_cmp_gt_u32_e64 s[8:9], 44, v196
	v_lshlrev_b32_e32 v196, 3, v196
	v_mul_lo_u32 v202, v202, s12
	s_cmp_gt_i32 s35, 63
	v_add_u32_e32 v202, 0, v202
	v_lshlrev_b32_e32 v203, 3, v203
	v_readlane_b32 s16, v195, 1
	s_cselect_b64 s[18:19], -1, 0
	s_cmp_lt_i32 s35, 64
	v_add_u32_e32 v204, s17, v196
	s_barrier
	s_cbranch_scc1 .LBB1_8
	s_waitcnt vmcnt(46)
	v_cvt_pk_f16_f32 v174, v174, v175
	v_cvt_pk_f16_f32 v175, v176, v177
	s_waitcnt vmcnt(44)
	v_cvt_pk_f16_f32 v166, v166, v167
	v_cvt_pk_f16_f32 v167, v168, v169
	ds_write2_b64 v204, v[174:175], v[166:167] offset0:156 offset1:231
	s_waitcnt vmcnt(43)
	v_cvt_pk_f16_f32 v166, v190, v191
	v_cvt_pk_f16_f32 v167, v192, v193
	s_waitcnt vmcnt(41)
	v_cvt_pk_f16_f32 v168, v182, v183
	v_cvt_pk_f16_f32 v169, v184, v185
	v_add_u32_e32 v174, 0x800, v204
	v_cvt_pk_f16_f32 v186, v186, v187
	v_cvt_pk_f16_f32 v187, v188, v189
	v_cvt_pk_f16_f32 v178, v178, v179
	v_cvt_pk_f16_f32 v179, v180, v181
	ds_write2_b64 v174, v[166:167], v[168:169] offset0:56 offset1:131
	v_cvt_pk_f16_f32 v166, v170, v171
	v_cvt_pk_f16_f32 v167, v172, v173
	s_waitcnt vmcnt(40)
	v_cvt_pk_f16_f32 v162, v162, v163
	v_cvt_pk_f16_f32 v163, v164, v165
	v_add_u32_e32 v164, 0xc00, v204
	ds_write2_b64 v204, v[186:187], v[178:179] offset1:75
	ds_write2_b64 v164, v[166:167], v[162:163] offset0:84 offset1:159
	s_and_saveexec_b64 s[12:13], s[8:9]
	s_cbranch_execz .LBB1_7
	s_waitcnt vmcnt(39)
	v_cvt_pk_f16_f32 v158, v158, v159
	v_cvt_pk_f16_f32 v159, v160, v161
	v_add_u32_e32 v160, v202, v203
	s_waitcnt vmcnt(38)
	v_cvt_pk_f16_f32 v154, v154, v155
	v_cvt_pk_f16_f32 v155, v156, v157
	ds_write2_b64 v160, v[158:159], v[154:155] offset1:75

.LBB1_8:
	s_and_b32 s12, s16, 0xff
	s_cmp_eq_u32 s12, 1
	s_cselect_b64 vcc, -1, 0
	s_and_b32 s12, s16, 0xff00
	s_cmpk_eq_i32 s12, 0x100
	s_cselect_b64 s[12:13], -1, 0
	s_and_b32 s14, s16, 0xff0000
	s_cmp_eq_u32 s14, 0x10000
	s_cselect_b64 s[14:15], -1, 0
	s_and_b32 s16, s16, 0xff000000
	s_cmp_eq_u32 s16, 0x1000000
	s_cselect_b64 s[16:17], -1, 0
	s_add_i32 s36, s34, 0x12c000
	s_waitcnt vmcnt(38)
	v_add_u32_e32 v154, s36, v194
	v_add_u32_e32 v155, s36, v197
	s_add_i32 s36, s34, 0x12c4b0
	v_cndmask_b32_e32 v154, v200, v154, vcc
	s_and_b64 vcc, vcc, s[10:11]
	v_add_u32_e32 v156, s36, v194
	s_mov_b32 s26, s22
	s_mov_b32 s27, s23
	v_cndmask_b32_e32 v155, v200, v155, vcc
	v_cndmask_b32_e64 v156, v200, v156, s[12:13]
	buffer_load_dwordx4 v[190:193], v154, s[20:23], 0 offen nt
	buffer_load_dwordx4 v[174:177], v156, s[20:23], 0 offen nt
	buffer_load_dwordx4 v[182:185], v154, s[24:27], 0 offen nt
	buffer_load_dwordx4 v[166:169], v156, s[24:27], 0 offen nt
	v_add_u32_e32 v154, s36, v197
	s_and_b64 vcc, s[12:13], s[2:3]
	s_add_i32 s12, s34, 0x12c960
	v_cndmask_b32_e32 v154, v155, v154, vcc
	v_add_u32_e32 v155, s12, v194
	v_add_u32_e32 v156, s12, v197
	s_and_b64 vcc, s[14:15], s[4:5]
	s_add_i32 s12, s34, 0x12ce10
	v_cndmask_b32_e64 v155, v200, v155, s[14:15]
	v_cndmask_b32_e32 v154, v154, v156, vcc
	v_add_u32_e32 v156, s12, v194
	v_cndmask_b32_e64 v156, v200, v156, s[16:17]
	buffer_load_dwordx4 v[186:189], v155, s[20:23], 0 offen nt
	buffer_load_dwordx4 v[170:173], v156, s[20:23], 0 offen nt
	buffer_load_dwordx4 v[178:181], v155, s[24:27], 0 offen nt
	buffer_load_dwordx4 v[162:165], v156, s[24:27], 0 offen nt
	v_add_u32_e32 v155, s12, v197
	s_and_b64 vcc, s[16:17], s[6:7]
	v_cndmask_b32_e32 v154, v154, v155, vcc
	buffer_load_dwordx4 v[158:161], v154, s[20:23], 0 offen nt
	s_nop 0
	buffer_load_dwordx4 v[154:157], v154, s[24:27], 0 offen nt
	v_mul_u32_u24_e32 v200, 0x4e0, v1
	v_mul_u32_u24_e32 v196, 0x440, v201
	v_readlane_b32 s16, v195, 2
	s_cmpk_lt_i32 s35, 0x80
	s_waitcnt lgkmcnt(0)
	s_barrier
	s_cbranch_scc1 .LBB1_12
	s_waitcnt vmcnt(8)
	v_cvt_pk_f16_f32 v174, v174, v175
	v_cvt_pk_f16_f32 v175, v176, v177
	s_waitcnt vmcnt(6)
	v_cvt_pk_f16_f32 v166, v166, v167
	v_cvt_pk_f16_f32 v167, v168, v169
	v_add_u32_e32 v168, 0x5000, v204
	ds_write2_b64 v168, v[174:175], v[166:167] offset0:92 offset1:167
	s_waitcnt vmcnt(5)
	v_cvt_pk_f16_f32 v166, v186, v187
	v_cvt_pk_f16_f32 v167, v188, v189
	s_waitcnt vmcnt(3)
	v_cvt_pk_f16_f32 v168, v178, v179
	v_cvt_pk_f16_f32 v169, v180, v181
	v_add_u32_e32 v174, 0x5400, v204
	v_cvt_pk_f16_f32 v190, v190, v191
	v_cvt_pk_f16_f32 v191, v192, v193
	v_cvt_pk_f16_f32 v182, v182, v183
	v_cvt_pk_f16_f32 v183, v184, v185
	v_add_u32_e32 v184, 0x4c00, v204
	ds_write2_b64 v174, v[166:167], v[168:169] offset0:120 offset1:195
	v_cvt_pk_f16_f32 v166, v170, v171
	v_cvt_pk_f16_f32 v167, v172, v173
	s_waitcnt vmcnt(2)
	v_cvt_pk_f16_f32 v162, v162, v163
	v_cvt_pk_f16_f32 v163, v164, v165
	v_add_u32_e32 v164, 0x5800, v204
	ds_write2_b64 v184, v[190:191], v[182:183] offset0:64 offset1:139
	ds_write2_b64 v164, v[166:167], v[162:163] offset0:148 offset1:223
	s_and_saveexec_b64 s[12:13], s[8:9]
	s_cbranch_execz .LBB1_11
	s_waitcnt vmcnt(1)
	v_cvt_pk_f16_f32 v158, v158, v159
	v_cvt_pk_f16_f32 v159, v160, v161
	v_add_u32_e32 v160, v202, v203
	s_waitcnt vmcnt(0)
	v_cvt_pk_f16_f32 v154, v154, v155
	v_cvt_pk_f16_f32 v155, v156, v157
	v_add_u32_e32 v156, 0x4c00, v160
	ds_write2_b64 v156, v[158:159], v[154:155] offset0:64 offset1:139

	.amdhsa_kernel _Z6k_gemmPKfS0_PK15HIP_vector_typeIjLj4EEPDF16_PKh
		.amdhsa_group_segment_fixed_size 0
		.amdhsa_private_segment_fixed_size 0
		.amdhsa_kernarg_size 40
		.amdhsa_user_sgpr_count 2
		.amdhsa_user_sgpr_dispatch_ptr 0
		.amdhsa_user_sgpr_queue_ptr 0
		.amdhsa_user_sgpr_kernarg_segment_ptr 1
		.amdhsa_user_sgpr_dispatch_id 0
		.amdhsa_user_sgpr_kernarg_preload_length 0
		.amdhsa_user_sgpr_kernarg_preload_offset 0
		.amdhsa_user_sgpr_private_segment_size 0
		.amdhsa_uses_dynamic_stack 0
		.amdhsa_enable_private_segment 0
		.amdhsa_system_sgpr_workgroup_id_x 1
		.amdhsa_system_sgpr_workgroup_id_y 0
		.amdhsa_system_sgpr_workgroup_id_z 0
		.amdhsa_system_sgpr_workgroup_info 0
		.amdhsa_system_vgpr_workitem_id 0
		.amdhsa_next_free_vgpr 230
		.amdhsa_next_free_sgpr 42
		.amdhsa_accum_offset 232
		.amdhsa_reserve_vcc 1
		.amdhsa_float_round_mode_32 0
		.amdhsa_float_round_mode_16_64 0
		.amdhsa_float_denorm_mode_32 3
		.amdhsa_float_denorm_mode_16_64 3
		.amdhsa_dx10_clamp 1
		.amdhsa_ieee_mode 1
		.amdhsa_fp16_overflow 0
		.amdhsa_tg_split 0
		.amdhsa_exception_fp_ieee_invalid_op 0
		.amdhsa_exception_fp_denorm_src 0
		.amdhsa_exception_fp_ieee_div_zero 0
		.amdhsa_exception_fp_ieee_overflow 0
		.amdhsa_exception_fp_ieee_underflow 0
		.amdhsa_exception_fp_ieee_inexact 0
		.amdhsa_exception_int_div_zero 0
	.end_amdhsa_kernel

amdhsa.kernels:
  - .agpr_count:     0
    .args:
      - .actual_access:  read_only
        .address_space:  global
        .offset:         0
        .size:           8
        .value_kind:     global_buffer
      - .actual_access:  read_only
        .address_space:  global
        .offset:         8
        .size:           8
        .value_kind:     global_buffer
      - .actual_access:  write_only
        .address_space:  global
        .offset:         16
        .size:           8
        .value_kind:     global_buffer
      - .actual_access:  write_only
        .address_space:  global
        .offset:         24
        .size:           8
        .value_kind:     global_buffer
      - .actual_access:  write_only
        .address_space:  global
        .offset:         32
        .size:           8
        .value_kind:     global_buffer
      - .actual_access:  write_only
        .address_space:  global
        .offset:         40
        .size:           8
        .value_kind:     global_buffer
    .group_segment_fixed_size: 32
    .kernarg_segment_align: 8
    .kernarg_segment_size: 48
    .language:       OpenCL C
    .language_version:
      - 2
      - 0
    .max_flat_workgroup_size: 512
    .name:           _Z6k_prepPKiPKfPiS3_P15HIP_vector_typeIjLj4EEPh
    .private_segment_fixed_size: 0
    .sgpr_count:     16
    .sgpr_spill_count: 0
    .symbol:         _Z6k_prepPKiPKfPiS3_P15HIP_vector_typeIjLj4EEPh.kd
    .uniform_work_group_size: 1
    .uses_dynamic_stack: false
    .vgpr_count:     24
    .vgpr_spill_count: 0
    .wavefront_size: 64
  - .agpr_count:     0
    .args:
      - .actual_access:  read_only
        .address_space:  global
        .offset:         0
        .size:           8
        .value_kind:     global_buffer
      - .actual_access:  read_only
        .address_space:  global
        .offset:         8
        .size:           8
        .value_kind:     global_buffer
      - .actual_access:  read_only
        .address_space:  global
        .offset:         16
        .size:           8
        .value_kind:     global_buffer
      - .actual_access:  write_only
        .address_space:  global
        .offset:         24
        .size:           8
        .value_kind:     global_buffer
      - .actual_access:  read_only
        .address_space:  global
        .offset:         32
        .size:           8
        .value_kind:     global_buffer
    .group_segment_fixed_size: 0
    .kernarg_segment_align: 8
    .kernarg_segment_size: 40
    .language:       OpenCL C
    .language_version:
      - 2
      - 0
    .max_flat_workgroup_size: 256
    .name:           _Z6k_gemmPKfS0_PK15HIP_vector_typeIjLj4EEPDF16_PKh
    .private_segment_fixed_size: 0
    .sgpr_count:     48
    .sgpr_spill_count: 0
    .symbol:         _Z6k_gemmPKfS0_PK15HIP_vector_typeIjLj4EEPDF16_PKh.kd
    .uniform_work_group_size: 1
    .uses_dynamic_stack: false
    .vgpr_count:     230
    .vgpr_spill_count: 0
    .wavefront_size: 64
  - .agpr_count:     0
    .args:
      - .actual_access:  read_only
        .address_space:  global
        .offset:         0
        .size:           8
        .value_kind:     global_buffer
      - .actual_access:  read_only
        .address_space:  global
        .offset:         8
        .size:           8
        .value_kind:     global_buffer
      - .actual_access:  read_only
        .address_space:  global
        .offset:         16
        .size:           8
        .value_kind:     global_buffer
      - .actual_access:  read_only
        .address_space:  global
        .offset:         24
        .size:           8
        .value_kind:     global_buffer
      - .actual_access:  read_only
        .address_space:  global
        .offset:         32
        .size:           8
        .value_kind:     global_buffer
      - .actual_access:  read_only
        .address_space:  global
        .offset:         40
        .size:           8
        .value_kind:     global_buffer
      - .actual_access:  write_only
        .address_space:  global
        .offset:         48
        .size:           8
        .value_kind:     global_buffer
    .group_segment_fixed_size: 4096
    .kernarg_segment_align: 8
    .kernarg_segment_size: 56
    .language:       OpenCL C
    .language_version:
      - 2
      - 0
    .max_flat_workgroup_size: 1024
    .name:           _Z6k_poolPKDF16_PKiS2_PKfS4_S4_Pf
    .private_segment_fixed_size: 0
    .sgpr_count:     20
    .sgpr_spill_count: 0
    .symbol:         _Z6k_poolPKDF16_PKiS2_PKfS4_S4_Pf.kd
    .uniform_work_group_size: 1
    .uses_dynamic_stack: false
    .vgpr_count:     60
    .vgpr_spill_count: 0
    .wavefront_size: 64
